# on top of v42: attention work-queue pull tries the own XCD queue's fetch-add directly (skips the preliminary head load), one round trip in the common case
# baseline (speedup 1.0000x reference)
; __global__ void __launch_bounds__(NTHREADS, 2) mk_fwd(Args args) {
;     ...
;         int item; Q2_PULL(item, CW_Q2, 64, 512);
.LBB0_370:
	v_cmp_eq_u32_e64 s[0:1], 0, v0
	s_barrier
	s_and_saveexec_b64 s[4:5], s[0:1]
	s_cbranch_execz .LBB0_411
	s_add_u32 s6, s30, 0x8500
	s_addc_u32 s7, s31, 0
	s_lshl_b32 s8, s2, 6
	s_and_b32 s8, s8, 0x1c0
	s_add_i32 s40, s2, 1
	v_mov_b32_e32 v1, s8
	s_lshl_b32 s8, s40, 6
	s_and_b32 s8, s8, 0x1c0
	s_add_i32 s39, s2, 2
	s_nop 0
	v_mov_b32_e32 v1, s8
	s_lshl_b32 s8, s39, 6
	s_and_b32 s8, s8, 0x1c0
	s_add_i32 s38, s2, 3
	global_load_dword v8, v1, s[6:7] sc1
	v_mov_b32_e32 v1, s8
	s_lshl_b32 s8, s38, 6
	s_and_b32 s8, s8, 0x1c0
	s_add_i32 s35, s2, 4
	global_load_dword v7, v1, s[6:7] sc1
	v_mov_b32_e32 v1, s8
	s_lshl_b32 s8, s35, 6
	s_and_b32 s8, s8, 0x1c0
	s_add_i32 s34, s2, 5
	global_load_dword v5, v1, s[6:7] sc1
	v_mov_b32_e32 v1, s8
	s_lshl_b32 s8, s34, 6
	s_and_b32 s8, s8, 0x1c0
	s_add_i32 s11, s2, 6
	global_load_dword v4, v1, s[6:7] sc1
	v_mov_b32_e32 v1, s8
	s_lshl_b32 s8, s11, 6
	s_and_b32 s8, s8, 0x1c0
	s_add_i32 s10, s2, 7
	global_load_dword v3, v1, s[6:7] sc1
	v_mov_b32_e32 v1, s8
	s_lshl_b32 s8, s10, 6
	s_and_b32 s8, s8, 0x1c0
	global_load_dword v2, v1, s[6:7] sc1
	v_mov_b32_e32 v1, s8
	global_load_dword v1, v1, s[6:7] sc1
	s_nop 0
	s_mov_b64 vcc, 0
	v_mov_b32_e32 v6, 0x200
	s_cbranch_vccnz .LBB0_375
	s_mov_b64 s[14:15], exec
	v_mbcnt_lo_u32_b32 v6, s14, 0
	v_mbcnt_hi_u32_b32 v6, s15, v6
	s_and_b32 s36, s2, 7
	v_cmp_eq_u32_e32 vcc, 0, v6
	s_and_saveexec_b64 s[8:9], vcc
	s_cbranch_execz .LBB0_374
	s_lshl_b32 s37, s36, 6
	s_bcnt1_i32_b64 s14, s[14:15]
	v_mov_b32_e32 v9, s37
	v_mov_b32_e32 v10, s14
	global_atomic_add v9, v9, v10, s[6:7] sc0

; __global__ void __launch_bounds__(NTHREADS, 2) mk_fwd(Args args) {
;     ...
;             Q2_PULL(item, CW_Q2, 64, 512);
.LBB0_486:
	s_barrier
	s_and_saveexec_b64 s[6:7], s[0:1]
	v_readlane_b32 s86, v254, 48
	v_readlane_b32 s87, v254, 49
	s_cbranch_execz .LBB0_415
	v_readlane_b32 s4, v255, 7
	v_readlane_b32 s5, v255, 8
	s_nop 4
	s_nop 0
	v_readlane_b32 s4, v255, 9
	v_readlane_b32 s5, v255, 10
	s_nop 0
	s_mov_b64 vcc, 0
	s_nop 2
	global_load_dword v9, v3, s[4:5] sc1
	v_readlane_b32 s4, v255, 11
	v_readlane_b32 s5, v255, 12
	s_and_b64 vcc, exec, vcc
	v_mov_b32_e32 v7, 0x200
	s_nop 2
	global_load_dword v8, v3, s[4:5] sc1
	v_readlane_b32 s4, v255, 13
	v_readlane_b32 s5, v255, 14
	s_nop 4
	global_load_dword v6, v3, s[4:5] sc1
	v_readlane_b32 s4, v255, 15
	v_readlane_b32 s5, v255, 16
	s_nop 4
	global_load_dword v5, v3, s[4:5] sc1
	v_readlane_b32 s4, v255, 17
	v_readlane_b32 s5, v255, 18
	s_nop 4
	global_load_dword v4, v3, s[4:5] sc1
	v_readlane_b32 s4, v255, 19
	v_readlane_b32 s5, v255, 20
	s_nop 4
	global_load_dword v2, v3, s[4:5] sc1
	v_readlane_b32 s4, v255, 21
	v_readlane_b32 s5, v255, 22
	s_nop 4
	global_load_dword v1, v3, s[4:5] sc1
	s_cbranch_vccnz .LBB0_491
	s_mov_b64 s[80:81], exec
	v_mbcnt_lo_u32_b32 v7, s80, 0
	v_mbcnt_hi_u32_b32 v7, s81, v7
	v_cmp_eq_u32_e32 vcc, 0, v7
	s_and_saveexec_b64 s[78:79], vcc
	s_cbranch_execz .LBB0_490
	s_bcnt1_i32_b64 s11, s[80:81]
	v_readlane_b32 s4, v255, 7
	v_mov_b32_e32 v10, s11
	v_readlane_b32 s5, v255, 8
	s_nop 4
	global_atomic_add v10, v3, v10, s[4:5] sc0

; __global__ void __launch_bounds__(NTHREADS, 2) mk_fwd(Args args) {
;     ...
;         Q2_PULL(item, CW_Q2 + 128, 128, 1024);
.LBB0_527:
	s_barrier
	s_and_saveexec_b64 s[4:5], s[0:1]
	s_cbranch_execz .LBB0_568
	s_add_u32 s6, s30, 0x8700
	s_addc_u32 s7, s31, 0
	s_lshl_b32 s8, s2, 6
	s_and_b32 s8, s8, 0x1c0
	s_add_i32 s41, s2, 1
	v_mov_b32_e32 v1, s8
	s_lshl_b32 s8, s41, 6
	s_and_b32 s8, s8, 0x1c0
	s_add_i32 s40, s2, 2
	s_nop 0
	v_mov_b32_e32 v1, s8
	s_lshl_b32 s8, s40, 6
	s_and_b32 s8, s8, 0x1c0
	s_add_i32 s39, s2, 3
	global_load_dword v8, v1, s[6:7] sc1
	v_mov_b32_e32 v1, s8
	s_lshl_b32 s8, s39, 6
	s_and_b32 s8, s8, 0x1c0
	s_add_i32 s35, s2, 4
	global_load_dword v7, v1, s[6:7] sc1
	v_mov_b32_e32 v1, s8
	s_lshl_b32 s8, s35, 6
	s_and_b32 s8, s8, 0x1c0
	s_add_i32 s34, s2, 5
	global_load_dword v5, v1, s[6:7] sc1
	v_mov_b32_e32 v1, s8
	s_lshl_b32 s8, s34, 6
	s_and_b32 s8, s8, 0x1c0
	s_add_i32 s11, s2, 6
	global_load_dword v4, v1, s[6:7] sc1
	v_mov_b32_e32 v1, s8
	s_lshl_b32 s8, s11, 6
	s_and_b32 s8, s8, 0x1c0
	s_add_i32 s10, s2, 7
	global_load_dword v3, v1, s[6:7] sc1
	v_mov_b32_e32 v1, s8
	s_lshl_b32 s8, s10, 6
	s_and_b32 s8, s8, 0x1c0
	global_load_dword v2, v1, s[6:7] sc1
	v_mov_b32_e32 v1, s8
	global_load_dword v1, v1, s[6:7] sc1
	s_movk_i32 s8, 0x7f
	s_nop 0
	s_mov_b64 vcc, 0
	v_mov_b32_e32 v6, 0x400
	s_cbranch_vccnz .LBB0_532
	s_mov_b64 s[14:15], exec
	v_mbcnt_lo_u32_b32 v6, s14, 0
	v_mbcnt_hi_u32_b32 v6, s15, v6
	s_and_b32 s36, s2, 7
	v_cmp_eq_u32_e32 vcc, 0, v6
	s_and_saveexec_b64 s[8:9], vcc
	s_cbranch_execz .LBB0_531
	s_lshl_b32 s37, s36, 6
	s_bcnt1_i32_b64 s14, s[14:15]
	v_mov_b32_e32 v9, s37
	v_mov_b32_e32 v10, s14
	global_atomic_add v9, v9, v10, s[6:7] sc0

; #define LAS __attribute__((address_space(3)))
; #define LDS_WAIT() asm volatile("s_waitcnt lgkmcnt(0)" ::: "memory")
; template <int D, bool MASK, bool BIAS, bool SINK, bool REV, bool O8, class BG>
; __device__ __forceinline__ void attn_unit(const Prm& P, LAS unsigned char* lds, BG& bg) {
;     ...
;     { auto rr = __builtin_amdgcn_permlane32_swap(__float_as_uint(l_reg), __float_as_uint(l_reg), false, false); l_reg = __uint_as_float(rr[0]) + __uint_as_float(rr[1]); }
;     if (hi == 0) wsf[32 + r32] = l_reg;
;     LDS_WAIT();
;     float rli[16];
; #pragma unroll
;     for (int g = 0; g < 4; ++g) { const f32x4 lv = *(const LAS f32x4*)(wsf + 32 + 8 * g + 4 * hi);
; #pragma unroll
;         for (int j = 0; j < 4; ++j) rli[4 * g + j] = __builtin_amdgcn_rcpf(lv[j]); }
;     __syncthreads();
;     int ln = lane; asm volatile("" : "+v"(ln));
;     const int r32e = ln & 31, hie = ln >> 5;
;     if constexpr (O8) {
;         LAS unsigned char* stg = lds + wid * (32 * D) + (4 * hie) * D + r32e;
; #pragma unroll
;         for (int r = 0; r < 16; ++r) { const int orow = (r & 3) + 8 * (r >> 2);
; #pragma unroll
;             for (int d = 0; d < NDB; ++d) { const float v = o[d][r] * rli[r]; stg[orow * D + d * 32] = (unsigned char)(__builtin_amdgcn_cvt_pk_fp8_f32(v, v, 0, false) & 0xff); } }
;         LDS_WAIT();
;         constexpr int CPR = D / 16, RPI = 64 / CPR;
;         const LAS unsigned char* stg2 = lds + wid * (32 * D) + (ln / CPR) * D + (ln % CPR) * 16;
;         unsigned char* Ow = (unsigned char*)P.O + (size_t)(wid * 32 + ln / CPR) * P.op + (ln % CPR) * 16;
; #pragma unroll
;         for (int i = 0; i < 32 / RPI; ++i) { const u32x4 v = *(const LAS u32x4*)(stg2 + i * RPI * D); *(u32x4*)(Ow + (size_t)(i * RPI) * P.op) = v; }
.LBB0_615:
	v_mov_b32_e32 v34, v87
	s_nop 1
	v_permlane32_swap_b32_e32 v87, v34
	s_and_saveexec_b64 s[6:7], s[4:5]
	v_add_f32_e32 v34, v87, v34
	v_lshl_add_u32 v35, v1, 2, s65
	ds_write_b32 v35, v34 offset:128
	s_or_b64 exec, exec, s[6:7]
	s_waitcnt lgkmcnt(0)
	v_add_u32_e32 v42, s65, v163
	ds_read_b128 v[34:37], v42 offset:128
	ds_read_b128 v[38:41], v42 offset:160
	s_add_u32 s6, s30, s74
	s_addc_u32 s7, s31, s75
	s_add_u32 s6, s6, s64
	s_waitcnt lgkmcnt(0)
	v_rcp_f32_e32 v43, v34
	v_rcp_f32_e32 v44, v35
	v_rcp_f32_e32 v45, v36
	v_rcp_f32_e32 v46, v37
	v_rcp_f32_e32 v47, v38
	ds_read_b128 v[34:37], v42 offset:192
	v_rcp_f32_e32 v48, v39
	v_rcp_f32_e32 v49, v40
	v_rcp_f32_e32 v50, v41
	ds_read_b128 v[38:41], v42 offset:224
	v_mov_b32_e32 v42, v190
	s_addc_u32 s7, s7, 0
	s_waitcnt vmcnt(0) lgkmcnt(0)
	s_barrier
	s_lshl_b32 s11, s96, 11
	v_lshlrev_b32_e32 v52, 3, v42
	v_and_b32_e32 v51, 31, v42
	s_add_i32 s11, s11, 0
	v_and_b32_e32 v52, 0xffffff00, v52
	v_add3_u32 v51, s11, v52, v51
	v_mul_f32_e32 v2, v2, v43
	v_mov_b32_e32 v52, v83
	v_cvt_pk_fp8_f32 v52, v2, v2
	v_mul_f32_e32 v2, v18, v43
	v_mov_b32_e32 v18, v83
	v_cvt_pk_fp8_f32 v18, v2, v2
	v_mul_f32_e32 v2, v3, v44
	v_mov_b32_e32 v3, v83
	v_cvt_pk_fp8_f32 v3, v2, v2
	v_mul_f32_e32 v2, v19, v44
	v_mov_b32_e32 v19, v83
	v_cvt_pk_fp8_f32 v19, v2, v2
	ds_write_b8 v51, v52
	ds_write_b8 v51, v18 offset:32
	ds_write_b8 v51, v3 offset:64
	ds_write_b8 v51, v19 offset:96
	v_mul_f32_e32 v2, v4, v45
	v_mov_b32_e32 v3, v83
	v_cvt_pk_fp8_f32 v3, v2, v2
	v_mul_f32_e32 v2, v20, v45
	v_mov_b32_e32 v4, v83
	v_cvt_pk_fp8_f32 v4, v2, v2
	v_mul_f32_e32 v2, v5, v46
	v_mov_b32_e32 v5, v83
	v_cvt_pk_fp8_f32 v5, v2, v2
	v_mul_f32_e32 v2, v21, v46
	v_mov_b32_e32 v18, v83
	v_cvt_pk_fp8_f32 v18, v2, v2
	ds_write_b8 v51, v3 offset:128
	ds_write_b8 v51, v4 offset:160
	ds_write_b8 v51, v5 offset:192
	ds_write_b8 v51, v18 offset:224
	v_mul_f32_e32 v2, v6, v47
	v_mov_b32_e32 v3, v83
	v_cvt_pk_fp8_f32 v3, v2, v2
	v_mul_f32_e32 v2, v22, v47
	v_mov_b32_e32 v4, v83
	v_cvt_pk_fp8_f32 v4, v2, v2
	v_mul_f32_e32 v2, v7, v48
	v_mov_b32_e32 v5, v83
	v_cvt_pk_fp8_f32 v5, v2, v2
	v_mul_f32_e32 v2, v23, v48
	v_mov_b32_e32 v6, v83
	v_cvt_pk_fp8_f32 v6, v2, v2
	ds_write_b8 v51, v3 offset:512
	ds_write_b8 v51, v4 offset:544
	ds_write_b8 v51, v5 offset:576
	ds_write_b8 v51, v6 offset:608
	v_mul_f32_e32 v2, v8, v49
	v_mov_b32_e32 v3, v83
	v_rcp_f32_e32 v34, v34
	v_cvt_pk_fp8_f32 v3, v2, v2
	v_mul_f32_e32 v2, v24, v49
	v_mov_b32_e32 v4, v83
	v_cvt_pk_fp8_f32 v4, v2, v2
	v_mul_f32_e32 v2, v9, v50
	v_mov_b32_e32 v5, v83
	v_rcp_f32_e32 v35, v35
	v_cvt_pk_fp8_f32 v5, v2, v2
	v_mul_f32_e32 v2, v25, v50
	v_mov_b32_e32 v6, v83
	v_cvt_pk_fp8_f32 v6, v2, v2
	ds_write_b8 v51, v3 offset:640
	ds_write_b8 v51, v4 offset:672
	ds_write_b8 v51, v5 offset:704
	ds_write_b8 v51, v6 offset:736
	v_mul_f32_e32 v2, v10, v34
	v_mov_b32_e32 v3, v83
	v_rcp_f32_e32 v36, v36
	v_cvt_pk_fp8_f32 v3, v2, v2
	v_mul_f32_e32 v2, v26, v34
	v_mov_b32_e32 v4, v83
	v_cvt_pk_fp8_f32 v4, v2, v2
	v_mul_f32_e32 v2, v11, v35
	v_mov_b32_e32 v5, v83
	v_rcp_f32_e32 v37, v37
	v_cvt_pk_fp8_f32 v5, v2, v2
	v_mul_f32_e32 v2, v27, v35
	v_mov_b32_e32 v6, v83
	v_cvt_pk_fp8_f32 v6, v2, v2
	ds_write_b8 v51, v3 offset:1024
	ds_write_b8 v51, v4 offset:1056
	ds_write_b8 v51, v5 offset:1088
	ds_write_b8 v51, v6 offset:1120
	v_mul_f32_e32 v2, v12, v36
	v_mov_b32_e32 v3, v83
	v_rcp_f32_e32 v38, v38
	v_cvt_pk_fp8_f32 v3, v2, v2
	v_mul_f32_e32 v2, v28, v36
	v_mov_b32_e32 v4, v83
	v_cvt_pk_fp8_f32 v4, v2, v2
	v_mul_f32_e32 v2, v13, v37
	v_mov_b32_e32 v5, v83
	v_rcp_f32_e32 v39, v39
	v_cvt_pk_fp8_f32 v5, v2, v2
	v_mul_f32_e32 v2, v29, v37
	v_mov_b32_e32 v6, v83
	v_cvt_pk_fp8_f32 v6, v2, v2
	ds_write_b8 v51, v3 offset:1152
	ds_write_b8 v51, v4 offset:1184
	ds_write_b8 v51, v5 offset:1216
	ds_write_b8 v51, v6 offset:1248
	v_mul_f32_e32 v2, v14, v38
	v_mov_b32_e32 v3, v83
	v_rcp_f32_e32 v40, v40
	v_cvt_pk_fp8_f32 v3, v2, v2
	v_mul_f32_e32 v2, v30, v38
	v_mov_b32_e32 v4, v83
	v_cvt_pk_fp8_f32 v4, v2, v2
	v_mul_f32_e32 v2, v15, v39
	v_mov_b32_e32 v5, v83
	v_rcp_f32_e32 v41, v41
	v_cvt_pk_fp8_f32 v5, v2, v2
	v_mul_f32_e32 v2, v31, v39
	v_mov_b32_e32 v6, v83
	v_cvt_pk_fp8_f32 v6, v2, v2
	ds_write_b8 v51, v3 offset:1536
	ds_write_b8 v51, v4 offset:1568
	ds_write_b8 v51, v5 offset:1600
	ds_write_b8 v51, v6 offset:1632
	v_mul_f32_e32 v2, v16, v40
	v_mov_b32_e32 v3, v83
	v_cvt_pk_fp8_f32 v3, v2, v2
	v_mul_f32_e32 v2, v32, v40
	v_mov_b32_e32 v4, v83
	v_cvt_pk_fp8_f32 v4, v2, v2
	v_mul_f32_e32 v2, v17, v41
	v_mov_b32_e32 v5, v83
	v_cvt_pk_fp8_f32 v5, v2, v2
	v_mul_f32_e32 v2, v33, v41
	v_mov_b32_e32 v6, v83
	v_cvt_pk_fp8_f32 v6, v2, v2
	v_ashrrev_i32_e32 v2, 31, v42
	v_lshrrev_b32_e32 v2, 30, v2
	v_add_u32_e32 v2, v42, v2
	ds_write_b8 v51, v3 offset:1664
	ds_write_b8 v51, v4 offset:1696
	ds_write_b8 v51, v5 offset:1728
	ds_write_b8 v51, v6 offset:1760
	v_ashrrev_i32_e32 v3, 2, v2
	v_and_b32_e32 v2, 0xffffffc, v2
	v_sub_u32_e32 v2, v42, v2
	v_lshlrev_b32_e32 v4, 6, v3
	v_lshlrev_b32_e32 v2, 4, v2
	v_add3_u32 v6, s11, v4, v2
	v_add_u32_e32 v4, s58, v3
	v_ashrrev_i32_e32 v5, 31, v4
	v_lshlrev_b64 v[4:5], 11, v[4:5]
	s_waitcnt lgkmcnt(0)
	v_lshl_add_u64 v[4:5], s[6:7], 0, v[4:5]
	v_ashrrev_i32_e32 v3, 31, v2
	v_lshl_add_u64 v[10:11], v[4:5], 0, v[2:3]
	ds_read_b128 v[2:5], v6
	s_mov_b32 s6, 0x12000000
	ds_read_b128 v[6:9], v6 offset:1024
	v_add_co_u32_e32 v12, vcc, s6, v10
	s_nop 1
	v_addc_co_u32_e32 v13, vcc, 0, v11, vcc
	s_waitcnt lgkmcnt(1)
	global_store_dwordx4 v[12:13], v[2:5], off offset:1024
	s_nop 1
	v_add_co_u32_e32 v2, vcc, 0x12008000, v10
	s_nop 1
	v_addc_co_u32_e32 v3, vcc, 0, v11, vcc
	s_waitcnt lgkmcnt(0)
	global_store_dwordx4 v[2:3], v[6:9], off offset:1024
	s_waitcnt lgkmcnt(0)
	s_barrier
	s_barrier
	s_and_saveexec_b64 s[6:7], s[0:1]
	s_cbranch_execz .LBB0_658
	v_readlane_b32 s40, v255, 0
	v_readlane_b32 s41, v255, 1
	s_nop 4
	s_nop 0
	global_load_dword v9, v83, s[72:73] sc1
	global_load_dword v8, v83, s[26:27] sc1
	global_load_dword v6, v83, s[20:21] sc1
	global_load_dword v5, v83, s[36:37] sc1
	global_load_dword v4, v83, s[48:49] sc1
	global_load_dword v3, v83, s[50:51] sc1
	global_load_dword v2, v83, s[56:57] sc1
	s_nop 0
	s_mov_b64 vcc, 0
	v_mov_b32_e32 v7, 0x400
	s_cbranch_vccnz .LBB0_622
	s_mov_b64 s[76:77], exec
	v_mbcnt_lo_u32_b32 v7, s76, 0
	v_mbcnt_hi_u32_b32 v7, s77, v7
	v_cmp_eq_u32_e32 vcc, 0, v7
	s_and_saveexec_b64 s[74:75], vcc
	s_cbranch_execz .LBB0_621
	s_bcnt1_i32_b64 s11, s[76:77]
	v_readlane_b32 s40, v255, 3
	v_mov_b32_e32 v10, s11
	v_readlane_b32 s41, v255, 4
	s_nop 4
	global_atomic_add v10, v83, v10, s[40:41] sc0
